# baseline (speedup 1.0000x reference)
.LBB1_33:
	s_cmp_gt_u32 s43, 22
	s_cselect_b64 s[38:39], -1, 0
	s_xor_b32 s8, s12, 1
	v_cmp_eq_u32_e64 s[4:5], -1, v190
	v_mov_b32_e32 v152, 0x44800000
	s_mulk_i32 s8, 0x4200
	v_add_u32_e32 v208, s8, v195
	v_lshl_add_u32 v144, v181, 1, v208
	v_cndmask_b32_e64 v152, v152, 0, s[4:5]
	v_fma_mixlo_f16 v141, v142, v152, 0
	v_fma_mixhi_f16 v141, v140, v152, 0
	s_cmp_lt_u32 s43, 23
	ds_write_b16 v144, v141
	ds_write_b16_d16_hi v144, v141 offset:8
	s_cbranch_scc1 .LBB1_35
	v_fma_mixlo_f16 v143, v142, v152, -v141 op_sel_hi:[0,0,1]
	v_fma_mixhi_f16 v143, v140, v152, -v141 op_sel:[0,0,1] op_sel_hi:[0,0,1]
	ds_write_b16 v144, v143 offset:8448
	ds_write_b16_d16_hi v144, v143 offset:8456
